# speedup vs baseline: 1.0270x; 1.0024x over previous
_Z8moe_gemmILi0EEvPKDF16_S1_PvPKyPKiPKfS1_:
	s_load_dwordx2 s[4:5], s[0:1], 0x18
	s_load_dwordx2 s[10:11], s[0:1], 0x20
	v_and_b32_e32 v1, 15, v0
	v_lshrrev_b32_e32 v2, 2, v1
	v_and_b32_e32 v3, 3, v1
	v_lshlrev_b32_e32 v2, 7, v2
	v_lshl_add_u32 v2, v3, 1, v2
	s_mov_b32 s12, 0x1c71c72
	s_waitcnt lgkmcnt(0)
	global_load_ushort v4, v2, s[4:5]
	global_load_ushort v5, v2, s[4:5] offset:512
	s_load_dwordx4 s[4:7], s[0:1], 0x0
	s_waitcnt vmcnt(0)
	v_add_u32_e32 v6, v4, v5
	v_add_u32_e32 v7, 0x8f, v6
	v_mul_hi_u32 v7, v7, s12
	v_mov_b32_e32 v8, v7
	s_nop 1
	v_add_u32_dpp v8, v8, v8 row_shr:1 row_mask:0xf bank_mask:0xf
	s_nop 1
	v_add_u32_dpp v8, v8, v8 row_shr:2 row_mask:0xf bank_mask:0xf
	s_nop 1
	v_add_u32_dpp v8, v8, v8 row_shr:4 row_mask:0xf bank_mask:0xf
	s_nop 1
	v_add_u32_dpp v8, v8, v8 row_shr:8 row_mask:0xf bank_mask:0xf
	s_nop 1
	v_readlane_b32 s15, v8, 15
	s_lshl_b32 s13, s15, 1
	s_cmp_ge_i32 s2, s13
	s_cbranch_scc1 .LBB2_132
	s_lshr_b32 s20, s15, 2
	s_and_b32 s21, s13, 6
	s_and_b32 s23, s2, 7
	s_add_i32 s24, s20, 1
	s_min_u32 s25, s23, s21
	s_mul_i32 s25, s25, s24
	s_sub_i32 s27, s23, s21
	s_max_i32 s27, s27, 0
	s_mul_i32 s27, s27, s20
	s_add_i32 s18, s25, s27
	s_ashr_i32 s28, s2, 3
	s_add_i32 s18, s18, s28
	s_ashr_i32 s22, s18, 1
	v_sub_u32_e32 v9, v8, v7
	v_cmp_le_i32_e64 s[28:29], v9, s22
	v_cmp_gt_i32_e64 s[30:31], v8, s22
	s_and_b64 s[28:29], s[28:29], s[30:31]
	s_ff1_i32_b64 s14, s[28:29]
	v_readlane_b32 s16, v4, s14
	v_readlane_b32 s17, v6, s14
	v_readlane_b32 s26, v7, s14
	v_readlane_b32 s27, v9, s14
	s_sub_i32 s2, s22, s27

_Z8moe_gemmILi1EEvPKDF16_S1_PvPKyPKiPKfS1_:
	s_load_dwordx2 s[4:5], s[0:1], 0x18
	s_load_dwordx2 s[8:9], s[0:1], 0x20
	v_and_b32_e32 v1, 15, v0
	v_lshrrev_b32_e32 v2, 2, v1
	v_and_b32_e32 v3, 3, v1
	v_lshlrev_b32_e32 v2, 7, v2
	v_lshl_add_u32 v2, v3, 1, v2
	s_mov_b32 s10, 0x1c71c72
	s_mov_b32 s11, 0x199999a
	s_waitcnt lgkmcnt(0)
	global_load_ushort v4, v2, s[4:5] offset:512
	s_load_dwordx4 s[4:7], s[0:1], 0x0
	s_waitcnt vmcnt(0)
	v_add_u32_e32 v5, 0x8f, v4
	v_add_u32_e32 v6, 0x9f, v4
	v_mul_hi_u32 v5, v5, s10
	v_mul_hi_u32 v6, v6, s11
	v_mov_b32_e32 v7, v5
	v_mov_b32_e32 v8, v6
	s_nop 1
	v_add_u32_dpp v7, v7, v7 row_shr:1 row_mask:0xf bank_mask:0xf
	v_add_u32_dpp v8, v8, v8 row_shr:1 row_mask:0xf bank_mask:0xf
	s_nop 1
	v_add_u32_dpp v7, v7, v7 row_shr:2 row_mask:0xf bank_mask:0xf
	v_add_u32_dpp v8, v8, v8 row_shr:2 row_mask:0xf bank_mask:0xf
	s_nop 1
	v_add_u32_dpp v7, v7, v7 row_shr:4 row_mask:0xf bank_mask:0xf
	v_add_u32_dpp v8, v8, v8 row_shr:4 row_mask:0xf bank_mask:0xf
	s_nop 1
	v_add_u32_dpp v7, v7, v7 row_shr:8 row_mask:0xf bank_mask:0xf
	v_add_u32_dpp v8, v8, v8 row_shr:8 row_mask:0xf bank_mask:0xf
	s_nop 1
	v_readlane_b32 s14, v7, 15
	v_readlane_b32 s15, v8, 15
	s_cmpk_lt_u32 s14, 0x41
	s_cselect_b64 s[10:11], -1, 0
	s_cselect_b32 s16, s14, s15
	s_lshl_b32 s17, s16, 2
	s_cmp_ge_i32 s2, s17
	s_cbranch_scc1 .LBB3_175
	s_lshr_b32 s20, s16, 1
	s_and_b32 s21, s17, 4
	s_and_b32 s22, s2, 7
	s_add_i32 s23, s20, 1
	s_min_u32 s24, s22, s21
	s_mul_i32 s24, s24, s23
	s_sub_i32 s25, s22, s21
	s_max_i32 s25, s25, 0
	s_mul_i32 s25, s25, s20
	s_add_i32 s18, s24, s25
	s_ashr_i32 s27, s2, 3
	s_add_i32 s18, s18, s27
	s_ashr_i32 s19, s18, 2
	v_cndmask_b32_e64 v9, v6, v5, s[10:11]
	v_cndmask_b32_e64 v10, v8, v7, s[10:11]
	v_sub_u32_e32 v11, v10, v9
	v_cmp_le_i32_e64 s[28:29], v11, s19
	v_cmp_gt_i32_e64 s[30:31], v10, s19
	s_and_b64 s[28:29], s[28:29], s[30:31]
	s_ff1_i32_b64 s13, s[28:29]
	v_readlane_b32 s12, v4, s13
	v_readlane_b32 s26, v9, s13
	v_readlane_b32 s27, v11, s13
	s_sub_i32 s2, s19, s27

_Z8moe_gemmILi2EEvPKDF16_S1_PvPKyPKiPKfS1_:
	s_load_dwordx2 s[4:5], s[0:1], 0x18
	s_load_dwordx2 s[8:9], s[0:1], 0x20
	v_and_b32_e32 v1, 15, v0
	v_lshrrev_b32_e32 v2, 2, v1
	v_and_b32_e32 v3, 3, v1
	v_lshlrev_b32_e32 v2, 7, v2
	v_lshl_add_u32 v2, v3, 1, v2
	s_mov_b32 s10, 0x1c71c72
	s_mov_b32 s11, 0x199999a
	s_waitcnt lgkmcnt(0)
	global_load_ushort v4, v2, s[4:5] offset:0
	s_load_dwordx4 s[4:7], s[0:1], 0x0
	s_waitcnt vmcnt(0)
	v_add_u32_e32 v5, 0x8f, v4
	v_add_u32_e32 v6, 0x9f, v4
	v_mul_hi_u32 v5, v5, s10
	v_mul_hi_u32 v6, v6, s11
	v_mov_b32_e32 v7, v5
	v_mov_b32_e32 v8, v6
	s_nop 1
	v_add_u32_dpp v7, v7, v7 row_shr:1 row_mask:0xf bank_mask:0xf
	v_add_u32_dpp v8, v8, v8 row_shr:1 row_mask:0xf bank_mask:0xf
	s_nop 1
	v_add_u32_dpp v7, v7, v7 row_shr:2 row_mask:0xf bank_mask:0xf
	v_add_u32_dpp v8, v8, v8 row_shr:2 row_mask:0xf bank_mask:0xf
	s_nop 1
	v_add_u32_dpp v7, v7, v7 row_shr:4 row_mask:0xf bank_mask:0xf
	v_add_u32_dpp v8, v8, v8 row_shr:4 row_mask:0xf bank_mask:0xf
	s_nop 1
	v_add_u32_dpp v7, v7, v7 row_shr:8 row_mask:0xf bank_mask:0xf
	v_add_u32_dpp v8, v8, v8 row_shr:8 row_mask:0xf bank_mask:0xf
	s_nop 1
	v_readlane_b32 s14, v7, 15
	v_readlane_b32 s15, v8, 15
	s_cmpk_lt_u32 s14, 0x41
	s_cselect_b64 s[10:11], -1, 0
	s_cselect_b32 s16, s14, s15
	s_lshl_b32 s17, s16, 2
	s_cmp_ge_i32 s2, s17
	s_cbranch_scc1 .LBB4_181
	s_lshr_b32 s20, s16, 1
	s_and_b32 s21, s17, 4
	s_and_b32 s22, s2, 7
	s_add_i32 s23, s20, 1
	s_min_u32 s24, s22, s21
	s_mul_i32 s24, s24, s23
	s_sub_i32 s25, s22, s21
	s_max_i32 s25, s25, 0
	s_mul_i32 s25, s25, s20
	s_add_i32 s18, s24, s25
	s_ashr_i32 s27, s2, 3
	s_add_i32 s18, s18, s27
	s_ashr_i32 s19, s18, 2
	v_cndmask_b32_e64 v9, v6, v5, s[10:11]
	v_cndmask_b32_e64 v10, v8, v7, s[10:11]
	v_sub_u32_e32 v11, v10, v9
	v_cmp_le_i32_e64 s[28:29], v11, s19
	v_cmp_gt_i32_e64 s[30:31], v10, s19
	s_and_b64 s[28:29], s[28:29], s[30:31]
	s_ff1_i32_b64 s13, s[28:29]
	v_readlane_b32 s12, v4, s13
	v_readlane_b32 s26, v9, s13
	v_readlane_b32 s27, v11, s13
	s_sub_i32 s2, s19, s27
